# staging loads of block-major steps run two pairs ahead (second register set = the wave's own Q fragments, reloaded at the last block-major join)
# baseline (speedup 1.0000x reference)
; #define LAS __attribute__((address_space(3)))
; __device__ __forceinline__ unsigned or_x16(unsigned u) { return u | __shfl_xor(u, 16); }
; __device__ __forceinline__ unsigned or_x32(unsigned u) { return u | __shfl_xor(u, 32); }
; __device__ __forceinline__ void select_blocks8(const LAS float* impw, LAS unsigned* mk, int lane, int cur, unsigned (&u)[2][4]) {
;     ...
; #pragma unroll
;     for (int c = 0; c < 2; ++c) {
;         if (i == 0) *(LAS u32x4*)(mk + (4 * c + k) * 4) = (u32x4){m4[c][0], m4[c][1], m4[c][2], m4[c][3]};
; #pragma unroll
;         for (int x = 0; x < 4; ++x) { unsigned v = m4[c][x]; v = or_x16(v); v = or_x32(v); u[c][x] = __builtin_amdgcn_readfirstlane(v); }
;     }
; __device__ __forceinline__ void nsa_unit(unsigned char* ws, LAS unsigned char* lds, const LAS float* lut, int b, int g, int tau, int tid_in) {
;     ...
;     __syncthreads();
; #pragma unroll
;     for (int c = 0; c < 2; ++c) { const float gc = NSA_GATE(c, 0);
; #pragma unroll
;         for (int dt = 0; dt < 4; ++dt) resw[(c * 4 + dt) * 64] = Oc[c][dt] * gc; }
.LBB0_1173:
	s_lshl_b32 s1, s91, 7
	s_add_i32 s24, s1, 0
	s_add_i32 s24, s24, 0x22d00
	v_cmp_eq_u32_e32 vcc, 0, v187
	v_add_u32_e32 v4, s24, v1
	s_and_saveexec_b64 s[6:7], vcc
	ds_write_b128 v4, v[74:77]
	s_or_b64 exec, exec, s[6:7]
	v_and_b32_e32 v5, 64, v176
	v_xor_b32_e32 v3, 16, v176
	v_add_u32_e32 v5, 64, v5
	v_cmp_lt_i32_e64 s[6:7], v3, v5
	v_xor_b32_e32 v78, 32, v176
	s_nop 0
	v_cndmask_b32_e64 v3, v176, v3, s[6:7]
	v_cmp_lt_i32_e64 s[6:7], v78, v5
	v_lshlrev_b32_e32 v3, 2, v3
	s_nop 0
	v_cndmask_b32_e64 v5, v176, v78, s[6:7]
	v_lshlrev_b32_e32 v155, 2, v5
	ds_bpermute_b32 v5, v3, v74
	s_waitcnt lgkmcnt(0)
	v_or_b32_e32 v5, v5, v74
	ds_bpermute_b32 v74, v155, v5
	s_waitcnt lgkmcnt(0)
	v_or_b32_e32 v5, v74, v5
	s_nop 0
	v_readfirstlane_b32 s17, v5
	ds_bpermute_b32 v5, v3, v75
	s_waitcnt lgkmcnt(0)
	v_or_b32_e32 v5, v5, v75
	ds_bpermute_b32 v74, v155, v5
	s_waitcnt lgkmcnt(0)
	v_or_b32_e32 v5, v74, v5
	s_nop 0
	v_readfirstlane_b32 s38, v5
	ds_bpermute_b32 v5, v3, v76
	s_waitcnt lgkmcnt(0)
	v_or_b32_e32 v5, v5, v76
	ds_bpermute_b32 v74, v155, v5
	s_waitcnt lgkmcnt(0)
	v_or_b32_e32 v5, v74, v5
	s_nop 0
	v_readfirstlane_b32 s39, v5
	ds_bpermute_b32 v5, v3, v77
	s_waitcnt lgkmcnt(0)
	v_or_b32_e32 v5, v5, v77
	ds_bpermute_b32 v74, v155, v5
	s_waitcnt lgkmcnt(0)
	v_or_b32_e32 v5, v74, v5
	s_nop 0
	v_readfirstlane_b32 s5, v5
	s_and_saveexec_b64 s[6:7], vcc
	ds_write_b128 v4, v[70:73] offset:64
	s_or_b64 exec, exec, s[6:7]
	ds_bpermute_b32 v4, v3, v70
	s_lshl_b32 s6, s2, 13
	s_mov_b32 s7, s27
	v_lshl_add_u64 v[158:159], s[6:7], 0, v[164:165]
	s_waitcnt lgkmcnt(0)
	v_or_b32_e32 v4, v4, v70
	ds_bpermute_b32 v5, v155, v4
	s_barrier
	s_waitcnt lgkmcnt(0)
	s_lshl_b32 s1, s91, 13
	s_add_i32 s1, s1, 0
	v_or_b32_e32 v74, v5, v4
	ds_bpermute_b32 v4, v3, v71
	v_lshl_add_u32 v1, v1, 4, s1
	v_add_u32_e32 v1, 0x10000, v1
	s_movk_i32 s1, 0x70
	s_andn2_b64 vcc, exec, s[50:51]
	s_waitcnt lgkmcnt(0)
	v_or_b32_e32 v4, v4, v71
	ds_bpermute_b32 v5, v155, v4
	s_waitcnt lgkmcnt(0)
	v_or_b32_e32 v75, v5, v4
	ds_bpermute_b32 v4, v3, v72
	v_readfirstlane_b32 s73, v75
	s_waitcnt lgkmcnt(0)
	v_or_b32_e32 v4, v4, v72
	ds_bpermute_b32 v5, v155, v4
	s_waitcnt lgkmcnt(0)
	v_or_b32_e32 v72, v5, v4
	ds_bpermute_b32 v4, v3, v73
	s_waitcnt lgkmcnt(0)
	v_or_b32_e32 v4, v4, v73
	ds_bpermute_b32 v5, v155, v4
	s_waitcnt lgkmcnt(0)
	v_or_b32_e32 v73, v5, v4
	v_mul_u32_u24_e32 v4, 3, v191
	v_lshlrev_b32_e32 v152, 2, v4
	v_lshl_add_u64 v[70:71], s[28:29], 0, v[152:153]
	v_mad_u64_u32 v[4:5], s[2:3], v158, s0, v[70:71]
	v_mad_i32_i24 v5, v159, s0, v5
	global_load_dword v4, v[4:5], off
	v_readfirstlane_b32 s72, v73
	s_waitcnt vmcnt(0)
	v_pk_mul_f32 v[212:213], v[56:57], v[4:5] op_sel_hi:[1,0]
	v_pk_mul_f32 v[210:211], v[54:55], v[4:5] op_sel_hi:[1,0]
	v_pk_mul_f32 v[216:217], v[60:61], v[4:5] op_sel_hi:[1,0]
	v_pk_mul_f32 v[214:215], v[58:59], v[4:5] op_sel_hi:[1,0]
	v_pk_mul_f32 v[220:221], v[64:65], v[4:5] op_sel_hi:[1,0]
	v_pk_mul_f32 v[218:219], v[62:63], v[4:5] op_sel_hi:[1,0]
	v_pk_mul_f32 v[224:225], v[68:69], v[4:5] op_sel_hi:[1,0]
	v_pk_mul_f32 v[222:223], v[66:67], v[4:5] op_sel_hi:[1,0]
	v_lshl_add_u64 v[4:5], s[6:7], 0, v[108:109]
	v_mad_u64_u32 v[54:55], s[2:3], v4, s0, v[70:71]
	v_mad_i32_i24 v55, v5, s0, v55
	global_load_dword v54, v[54:55], off
	v_readfirstlane_b32 s2, v74
	v_readfirstlane_b32 s3, v72
	s_waitcnt vmcnt(0)
	v_pk_mul_f32 v[228:229], v[40:41], v[54:55] op_sel_hi:[1,0]
	v_pk_mul_f32 v[226:227], v[38:39], v[54:55] op_sel_hi:[1,0]
	v_pk_mul_f32 v[232:233], v[44:45], v[54:55] op_sel_hi:[1,0]
	v_pk_mul_f32 v[230:231], v[42:43], v[54:55] op_sel_hi:[1,0]
	v_pk_mul_f32 v[236:237], v[48:49], v[54:55] op_sel_hi:[1,0]
	v_pk_mul_f32 v[234:235], v[46:47], v[54:55] op_sel_hi:[1,0]
	v_pk_mul_f32 v[240:241], v[52:53], v[54:55] op_sel_hi:[1,0]
	v_pk_mul_f32 v[238:239], v[50:51], v[54:55] op_sel_hi:[1,0]
	s_mov_b32 s98, 0
	s_mov_b32 s100, -1
	s_mov_b32 s101, 0
	s_mov_b32 s99, 0
	v_and_b32_e32 v248, 3, v185
	v_lshlrev_b32_e32 v249, 2, v248
	v_lshl_add_u32 v248, v186, 6, v249
	v_add_u32_e32 v248, 0x10000, v248
	v_add_u32_e32 v249, 0x20400, v249
	v_lshlrev_b32_e32 v250, 2, v184
	v_and_b32_e32 v251, 63, v185
	v_lshlrev_b32_e32 v251, 4, v251
	v_add_u32_e32 v251, 0x22d00, v251
	ds_read_b128 v[242:245], v251
	s_waitcnt lgkmcnt(0)
	v_xor_b32_e32 v39, v110, v185
	v_lshlrev_b32_e32 v38, 7, v110
	v_lshlrev_b32_e32 v39, 4, v39
	v_and_or_b32 v38, v39, s1, v38
	v_add_u32_e32 v188, 0, v38
	v_cndmask_b32_e64 v38, 0, 1, s[50:51]
	v_cmp_ne_u32_e64 s[6:7], 1, v38
	ds_write_b128 v188, v[26:29]
	ds_write_b128 v188, v[22:25] offset:32768
	s_cbranch_vccnz .LBB0_1179
	ds_write_b128 v188, v[30:33] offset:8192
	ds_write_b128 v188, v[34:37] offset:40960

.LBB0_1183:
	s_add_i32 s76, s75, 2
	s_cmp_gt_i32 s76, s37
	s_cselect_b64 s[66:67], -1, 0
	s_cmp_le_i32 s76, s37
	s_cselect_b64 s[68:69], -1, 0
	s_and_b64 s[12:13], s[66:67], exec
	s_cselect_b32 s13, s79, s65
	s_cselect_b32 s12, s54, s64
	s_cselect_b32 s15, s36, s63
	s_cselect_b32 s14, s51, s62
	s_cmp_eq_u32 s99, 0
	s_cbranch_scc1 .Lbm_top_loads
	s_cmp_eq_u32 s99, 1
	s_cselect_b32 s99, 0, s99
	s_add_i32 s11, s75, 3
	s_cmp_le_i32 s11, s37
	s_cselect_b64 s[70:71], -1, 0
	s_branch .LBB0_1185

.LBB0_1185:
	s_cmp_lt_u32 s75, 2
	s_cbranch_scc1 .Lbm_old
	s_cmp_gt_i32 s75, s26
	s_cbranch_scc0 .Lbm_step
	s_cmp_eq_u32 s98, 0
	s_cbranch_scc1 .Lbm_old
	s_mul_i32 s11, s91, 8320
	v_mul_u32_u24_e32 v79, 260, v250
	v_add3_u32 v79, v79, s11, v248
	v_lshlrev_b32_e32 v80, 6, v186
	v_sub_u32_e32 v80, v79, v80
	ds_read_b32 v70, v79 offset:0
	ds_read_b32 v71, v79 offset:16
	ds_read_b32 v72, v79 offset:32
	ds_read_b32 v73, v79 offset:48
	ds_read_b32 v66, v79 offset:256
	ds_read_b32 v67, v79 offset:272
	ds_read_b32 v68, v79 offset:288
	ds_read_b32 v69, v79 offset:304
	ds_read_b32 v62, v79 offset:512
	ds_read_b32 v63, v79 offset:528
	ds_read_b32 v64, v79 offset:544
	ds_read_b32 v65, v79 offset:560
	s_waitcnt lgkmcnt(0)
	ds_read_b32 v54, v79 offset:768
	ds_read_b32 v55, v79 offset:784
	ds_read_b32 v56, v79 offset:800
	ds_read_b32 v57, v79 offset:816
	ds_read_b32 v50, v79 offset:4160
	ds_read_b32 v51, v79 offset:4176
	ds_read_b32 v52, v79 offset:4192
	ds_read_b32 v53, v79 offset:4208
	ds_read_b32 v46, v79 offset:4416
	ds_read_b32 v47, v79 offset:4432
	ds_read_b32 v48, v79 offset:4448
	ds_read_b32 v49, v79 offset:4464
	s_waitcnt lgkmcnt(0)
	ds_read_b32 v42, v79 offset:4672
	ds_read_b32 v43, v79 offset:4688
	ds_read_b32 v44, v79 offset:4704
	ds_read_b32 v45, v79 offset:4720
	ds_read_b32 v38, v79 offset:4928
	ds_read_b32 v39, v79 offset:4944
	ds_read_b32 v40, v79 offset:4960
	ds_read_b32 v41, v79 offset:4976
	ds_read_b32 v74, v80 offset:1024
	ds_read_b32 v58, v80 offset:5184
	s_waitcnt lgkmcnt(0)
	v_mov_b32_e32 v75, v74
	v_mov_b32_e32 v76, v74
	v_mov_b32_e32 v77, v74
	v_mov_b32_e32 v59, v58
	v_mov_b32_e32 v60, v58
	v_mov_b32_e32 v61, v58
	s_bitcmp1_b32 s26, 0
	s_cbranch_scc1 .Lbm_hk4
	s_waitcnt vmcnt(2)
	s_branch .Lbm_hkd
.Lbm_hk4:
	s_waitcnt vmcnt(4)
.Lbm_hkd:
	s_mov_b32 s98, 0

.Lbm_step:
	s_mov_b32 s98, 1
	s_cmp_eq_u32 s100, s75
	s_cbranch_scc0 .Lbm_slow
	s_and_b32 s83, s1, 0x4000
	v_mov_b32_e32 v112, s20
	v_mov_b32_e32 v113, s20
	v_mov_b32_e32 v114, s20
	v_mov_b32_e32 v115, s20
	v_lshrrev_b32_e32 v56, 31, v251
	v_xor_b32_e32 v56, 1, v56
	v_max_i32_e32 v55, 0, v251
	v_mov_b32_e32 v79, v56
	v_and_b32_e32 v54, 63, v55
	v_bfe_u32 v58, v55, 6, 1
	v_bfe_u32 v59, v55, 7, 1
	v_lshl_add_u32 v63, v54, 4, v249
	ds_read_b32 v199, v63
	v_mul_u32_u24_e32 v83, 0x410, v54
	v_cmp_ne_u32_e32 vcc, 0, v58
	v_add_u32_e32 v83, v83, v248
	s_nop 0
	v_cndmask_b32_e32 v81, v2, v154, vcc
	s_cmp_lg_u64 vcc, 0
	s_cselect_b32 s21, 1, 0
	v_cmp_ne_u32_e32 vcc, 0, v59
	s_nop 1
	v_cndmask_b32_e32 v82, v2, v154, vcc
	s_cmp_lg_u64 vcc, 0
	s_cselect_b32 s32, 1, 0
	s_cmp_eq_u32 s101, 4
	s_cbranch_scc1 .Lbm_q4_f
	s_cmp_eq_u32 s101, 8
	s_cbranch_scc1 .Lbm_q8_f
	s_waitcnt vmcnt(0)
	s_branch .Lbm_qd_f
.Lbm_q8_f:
	s_waitcnt vmcnt(8)
	s_branch .Lbm_qd_f

.Lbm_qd_f:
	s_and_b32 s77, s21, s32
	s_cmp_eq_u32 s77, 1
	s_cbranch_scc1 .Lbm_full_f
	s_mov_b32 s77, s83
	s_cmp_eq_u32 s21, 1
	s_cbranch_scc1 .Lbm_half_f
	s_add_i32 s77, s1, 0x2000
	s_and_b32 s77, s77, 0x6000
	v_mov_b32_e32 v81, v82

; __device__ __forceinline__ float ex2(float x) { return __builtin_amdgcn_exp2f(x); }
; template <bool SELMASK>
; __device__ __forceinline__ void attn_far_fast(const LAS unsigned char* kb, const LAS unsigned char* vb, const bf16x8 (&qf)[2][2], int col, int q, float bias_far, bool sel0, bool sel1, Softmax (&st)[2], f32x4 (&O)[2][4]) {
;     ...
; #pragma unroll
;     for (int kt = 0; kt < 4; ++kt) { const bf16x8 k0 = lds_frag(kb, 16 * kt + col, q), k1 = lds_frag(kb, 16 * kt + col, 4 + q);
; #pragma unroll
;         for (int c = 0; c < 2; ++c) { S[c][kt] = __builtin_amdgcn_mfma_f32_16x16x32_bf16(k0, qf[c][0], z4, 0, 0, 0); S[c][kt] = __builtin_amdgcn_mfma_f32_16x16x32_bf16(k1, qf[c][1], S[c][kt], 0, 0, 0); } }
;     bf16x8 pf[2][2];
; #pragma unroll
;     for (int c = 0; c < 2; ++c) {
;         const bool sel = c == 0 ? sel0 : sel1;
;         const float off = ((SELMASK && !sel) ? NEG : bias_far) - st[c].m;
; #pragma unroll
;         for (int kt = 0; kt < 4; ++kt) { f32x4 p = S[c][kt] + off;
; #pragma unroll
;             for (int e = 0; e < 4; ++e) p[e] = ex2(p[e]);
;             S[c][kt] = p; }
;         pf[c][0] = pack8(S[c][0], S[c][1]); pf[c][1] = pack8(S[c][2], S[c][3]);
;         st[c].l = __builtin_amdgcn_mfma_f32_16x16x32_bf16(ONES8, pf[c][0], st[c].l, 0, 0, 0); st[c].l = __builtin_amdgcn_mfma_f32_16x16x32_bf16(ONES8, pf[c][1], st[c].l, 0, 0, 0);
;     }
.Lbm_full_f:
	v_add_u32_e32 v148, s83, v192
	v_add_u32_e32 v149, v148, v195
	v_add_u32_e32 v148, v148, v193
	ds_read_b128 v[116:119], v148
	ds_read_b128 v[120:123], v149
	ds_read_b128 v[124:127], v148 offset:2048
	ds_read_b128 v[128:131], v149 offset:2048
	ds_read_b128 v[132:135], v148 offset:4096
	ds_read_b128 v[136:139], v149 offset:4096
	ds_read_b128 v[140:143], v148 offset:6144
	ds_read_b128 v[144:147], v149 offset:6144
	s_add_i32 s32, s1, 0x2000
	s_and_b32 s32, s32, 0x6000
	v_add_u32_e32 v208, s32, v192
	v_add_u32_e32 v209, v208, v195
	v_add_u32_e32 v208, v208, v193
	ds_read_b128 v[38:41], v208
	ds_read_b128 v[42:45], v209
	ds_read_b128 v[46:49], v208 offset:2048
	ds_read_b128 v[50:53], v209 offset:2048
	s_waitcnt lgkmcnt(12)
	v_sub_f32_e32 v81, v81, v199
	v_sub_f32_e32 v82, v82, v199
	v_mov_b32_e32 v70, v81
	v_mov_b32_e32 v71, v81
	v_mov_b32_e32 v72, v81
	v_mov_b32_e32 v73, v81
	v_mov_b32_e32 v74, v81
	v_mov_b32_e32 v75, v81
	v_mov_b32_e32 v76, v81
	v_mov_b32_e32 v77, v81
	v_mov_b32_e32 v200, v81
	v_mov_b32_e32 v201, v81
	v_mov_b32_e32 v202, v81
	v_mov_b32_e32 v203, v81
	v_mov_b32_e32 v204, v81
	v_mov_b32_e32 v205, v81
	v_mov_b32_e32 v206, v81
	v_mov_b32_e32 v207, v81
	v_mov_b32_e32 v54, v82
	v_mov_b32_e32 v55, v82
	v_mov_b32_e32 v56, v82
	v_mov_b32_e32 v57, v82
	v_mov_b32_e32 v58, v82
	v_mov_b32_e32 v59, v82
	v_mov_b32_e32 v60, v82
	v_mov_b32_e32 v61, v82
	v_mov_b32_e32 v62, v82
	v_mov_b32_e32 v63, v82
	v_mov_b32_e32 v64, v82
	v_mov_b32_e32 v65, v82
	v_mov_b32_e32 v66, v82
	v_mov_b32_e32 v67, v82
	v_mov_b32_e32 v68, v82
	v_mov_b32_e32 v69, v82
	s_mov_b32 s83, -1
	s_add_i32 s77, s75, 2
	s_cmp_gt_i32 s77, s26
	s_cbranch_scc1 .Lbm_g1_end_af
	s_lshr_b32 s21, s77, 5
	v_mov_b32_e32 v255, v242
	s_cmp_eq_u32 s21, 1
	s_cselect_b64 vcc, -1, 0
	v_cndmask_b32_e32 v255, v255, v243, vcc
	s_cmp_eq_u32 s21, 2
	s_cselect_b64 vcc, -1, 0
	v_cndmask_b32_e32 v255, v255, v244, vcc
	s_cmp_eq_u32 s21, 3
	s_cselect_b64 vcc, -1, 0
	v_cndmask_b32_e32 v255, v255, v245, vcc
	s_and_b32 s21, s77, 31
	s_lshl_b32 s21, 1, s21
	s_lshl_b32 s32, s21, 1
	v_and_b32_e32 v80, s21, v255
	v_cmp_ne_u32_e64 s[12:13], 0, v80
	v_and_b32_e32 v80, s32, v255
	v_cmp_ne_u32_e64 s[14:15], 0, v80
	s_nop 3
	s_or_b64 s[22:23], s[12:13], s[14:15]
	s_bcnt1_i32_b64 s11, s[22:23]
	s_add_i32 s11, s11, 3
	s_lshr_b32 s11, s11, 2
	s_cmp_ge_u32 s91, s11
	s_cbranch_scc1 .Lbm_g1_end_af
	s_add_i32 s83, s91, 8
	s_cmp_lt_u32 s83, s11
	s_cselect_b32 s83, 0x10000, 0
	s_add_i32 s83, s83, s75
	s_add_i32 s83, s83, 2
	s_andn2_b64 s[84:85], s[12:13], s[14:15]
	s_bcnt1_i32_b64 s77, s[84:85]
	v_mbcnt_lo_u32_b32 v80, s84, 0
	v_mbcnt_hi_u32_b32 v80, s85, v80
	v_mov_b32_e32 v255, s77
	s_and_b64 s[84:85], s[12:13], s[14:15]
	s_bcnt1_i32_b64 s32, s[84:85]
	v_mbcnt_lo_u32_b32 v255, s84, v255
	v_mbcnt_hi_u32_b32 v255, s85, v255
	s_add_i32 s77, s77, s32
	v_cndmask_b32_e64 v80, v80, v255, s[84:85]
	v_mov_b32_e32 v255, s77
	s_andn2_b64 s[84:85], s[14:15], s[12:13]
	v_mbcnt_lo_u32_b32 v255, s84, v255
	v_mbcnt_hi_u32_b32 v255, s85, v255
	s_nop 0
	v_cndmask_b32_e64 v80, v80, v255, s[84:85]
	v_cndmask_b32_e64 v78, 0, 1, s[12:13]
	v_cndmask_b32_e64 v255, 0, 2, s[14:15]
	v_or_b32_e32 v78, v78, v255
	v_and_b32_e32 v255, 63, v185
	v_lshl_or_b32 v78, v78, 6, v255
	s_lshl_b32 s77, s91, 6
	s_add_i32 s77, s77, 0x20900
	v_add_u32_e32 v255, s77, v80
	s_and_saveexec_b64 s[84:85], s[22:23]
	ds_write_b8 v255, v78
	s_mov_b64 exec, s[84:85]
	s_lshl_b32 s32, s91, 2
	s_bcnt1_i32_b64 s84, s[22:23]
	v_lshrrev_b32_e32 v78, 2, v250
	v_add_u32_e32 v78, s32, v78
	v_cmp_gt_u32_e32 vcc, s84, v78
	v_add_u32_e32 v255, s77, v78
	ds_read_u8 v251, v255
	v_cndmask_b32_e64 v254, -1, 0, vcc

.Lbm_slow:
	s_lshr_b32 s21, s75, 5
	v_mov_b32_e32 v79, v242
	s_cmp_eq_u32 s21, 1
	s_cselect_b64 vcc, -1, 0
	v_cndmask_b32_e32 v79, v79, v243, vcc
	s_cmp_eq_u32 s21, 2
	s_cselect_b64 vcc, -1, 0
	v_cndmask_b32_e32 v79, v79, v244, vcc
	s_cmp_eq_u32 s21, 3
	s_cselect_b64 vcc, -1, 0
	v_cndmask_b32_e32 v79, v79, v245, vcc
	s_and_b32 s21, s75, 31
	s_lshl_b32 s21, 1, s21
	s_lshl_b32 s32, s21, 1
	v_and_b32_e32 v80, s21, v79
	v_cmp_ne_u32_e64 s[12:13], 0, v80
	v_and_b32_e32 v80, s32, v79
	v_cmp_ne_u32_e64 s[14:15], 0, v80
	s_nop 3
	s_or_b64 s[22:23], s[12:13], s[14:15]
	s_bcnt1_i32_b64 s11, s[22:23]
	s_add_i32 s11, s11, 3
	s_lshr_b32 s11, s11, 2
	s_cmp_ge_u32 s91, s11
	s_cbranch_scc1 .Lbm_noitem
	s_and_b32 s83, s1, 0x4000
	v_mov_b32_e32 v112, s20
	v_mov_b32_e32 v113, s20
	v_mov_b32_e32 v114, s20
	v_mov_b32_e32 v115, s20
	s_add_i32 s10, s91, 8
	s_cmp_lt_u32 s10, s11
	s_cselect_b32 s10, 1, 0
	s_and_b32 s77, s100, 0xffff
	s_cmp_eq_u32 s77, s75
	s_cbranch_scc1 .Lbm_r1_pf
	s_andn2_b64 s[84:85], s[12:13], s[14:15]
	s_bcnt1_i32_b64 s77, s[84:85]
	v_mbcnt_lo_u32_b32 v80, s84, 0
	v_mbcnt_hi_u32_b32 v80, s85, v80
	v_mov_b32_e32 v56, s77
	s_and_b64 s[84:85], s[12:13], s[14:15]
	s_bcnt1_i32_b64 s32, s[84:85]
	v_mbcnt_lo_u32_b32 v56, s84, v56
	v_mbcnt_hi_u32_b32 v56, s85, v56
	s_add_i32 s77, s77, s32
	v_cndmask_b32_e64 v80, v80, v56, s[84:85]
	v_mov_b32_e32 v56, s77
	s_andn2_b64 s[84:85], s[14:15], s[12:13]
	v_mbcnt_lo_u32_b32 v56, s84, v56
	v_mbcnt_hi_u32_b32 v56, s85, v56
	s_nop 0
	v_cndmask_b32_e64 v80, v80, v56, s[84:85]
	v_cndmask_b32_e64 v58, 0, 1, s[12:13]
	v_cndmask_b32_e64 v59, 0, 2, s[14:15]
	v_or_b32_e32 v58, v58, v59
	v_and_b32_e32 v59, 63, v185
	v_lshl_or_b32 v58, v58, 6, v59
	s_lshl_b32 s77, s91, 6
	s_add_i32 s77, s77, 0x20900
	v_add_u32_e32 v59, s77, v80
	s_and_saveexec_b64 s[84:85], s[22:23]
	ds_write_b8 v59, v58
	s_mov_b64 exec, s[84:85]
	s_lshl_b32 s32, s91, 2
	s_bcnt1_i32_b64 s84, s[22:23]
	v_lshrrev_b32_e32 v58, 2, v250
	v_add_u32_e32 v58, s32, v58
	v_cmp_gt_u32_e32 vcc, s84, v58
	v_add_u32_e32 v59, s77, v58
	ds_read_u8 v63, v59
	v_cndmask_b32_e64 v60, -1, 0, vcc
	s_waitcnt lgkmcnt(0)
	v_or_b32_e32 v63, v63, v60
	v_lshrrev_b32_e32 v56, 31, v63
	v_xor_b32_e32 v56, 1, v56
	v_max_i32_e32 v55, 0, v63
	v_mov_b32_e32 v79, v56
	v_and_b32_e32 v54, 63, v55
	v_bfe_u32 v58, v55, 6, 1
	v_bfe_u32 v59, v55, 7, 1
	v_lshlrev_b32_e32 v60, 11, v54
	v_mov_b32_e32 v61, 0
	v_lshl_add_u64 v[60:61], v[60:61], 0, v[246:247]
	global_load_dwordx4 v[104:107], v[60:61], off
	global_load_dwordx4 v[108:111], v[60:61], off offset:64
	v_lshl_add_u32 v63, v54, 4, v249
	ds_read_b32 v199, v63
	v_mul_u32_u24_e32 v83, 0x410, v54
	v_cmp_ne_u32_e32 vcc, 0, v58
	v_add_u32_e32 v83, v83, v248
	s_nop 0
	v_cndmask_b32_e32 v81, v2, v154, vcc
	s_cmp_lg_u64 vcc, 0
	s_cselect_b32 s21, 1, 0
	v_cmp_ne_u32_e32 vcc, 0, v59
	s_nop 1
	v_cndmask_b32_e32 v82, v2, v154, vcc
	s_cmp_lg_u64 vcc, 0
	s_cselect_b32 s32, 1, 0
	s_waitcnt vmcnt(0)
	s_branch .Lbm_r1_go
.Lbm_r1_pf:
	v_lshrrev_b32_e32 v56, 31, v251
	v_xor_b32_e32 v56, 1, v56
	v_max_i32_e32 v55, 0, v251
	v_mov_b32_e32 v79, v56
	v_and_b32_e32 v54, 63, v55
	v_bfe_u32 v58, v55, 6, 1
	v_bfe_u32 v59, v55, 7, 1
	v_lshl_add_u32 v63, v54, 4, v249
	ds_read_b32 v199, v63
	v_mul_u32_u24_e32 v83, 0x410, v54
	v_cmp_ne_u32_e32 vcc, 0, v58
	v_add_u32_e32 v83, v83, v248
	s_nop 0
	v_cndmask_b32_e32 v81, v2, v154, vcc
	s_cmp_lg_u64 vcc, 0
	s_cselect_b32 s21, 1, 0
	v_cmp_ne_u32_e32 vcc, 0, v59
	s_nop 1
	v_cndmask_b32_e32 v82, v2, v154, vcc
	s_cmp_lg_u64 vcc, 0
	s_cselect_b32 s32, 1, 0
	s_cmp_eq_u32 s101, 4
	s_cbranch_scc1 .Lbm_q4_s
	s_cmp_eq_u32 s101, 8
	s_cbranch_scc1 .Lbm_q8_s
	s_waitcnt vmcnt(0)
	s_branch .Lbm_qd_s

.Lbm_qd_s:
.Lbm_r1_go:
	s_cmp_eq_u32 s10, 1
	s_cbranch_scc1 .Lbm_r1_two
	s_and_b32 s77, s21, s32
	s_cmp_eq_u32 s77, 1
	s_cbranch_scc1 .Lbm_full_s
	s_mov_b32 s77, s83
	s_cmp_eq_u32 s21, 1
	s_cbranch_scc1 .Lbm_half_s
	s_add_i32 s77, s1, 0x2000
	s_and_b32 s77, s77, 0x6000
	v_mov_b32_e32 v81, v82

; __device__ __forceinline__ float ex2(float x) { return __builtin_amdgcn_exp2f(x); }
; template <bool SELMASK>
; __device__ __forceinline__ void attn_far_fast(const LAS unsigned char* kb, const LAS unsigned char* vb, const bf16x8 (&qf)[2][2], int col, int q, float bias_far, bool sel0, bool sel1, Softmax (&st)[2], f32x4 (&O)[2][4]) {
;     ...
; #pragma unroll
;     for (int kt = 0; kt < 4; ++kt) { const bf16x8 k0 = lds_frag(kb, 16 * kt + col, q), k1 = lds_frag(kb, 16 * kt + col, 4 + q);
; #pragma unroll
;         for (int c = 0; c < 2; ++c) { S[c][kt] = __builtin_amdgcn_mfma_f32_16x16x32_bf16(k0, qf[c][0], z4, 0, 0, 0); S[c][kt] = __builtin_amdgcn_mfma_f32_16x16x32_bf16(k1, qf[c][1], S[c][kt], 0, 0, 0); } }
;     bf16x8 pf[2][2];
; #pragma unroll
;     for (int c = 0; c < 2; ++c) {
;         const bool sel = c == 0 ? sel0 : sel1;
;         const float off = ((SELMASK && !sel) ? NEG : bias_far) - st[c].m;
; #pragma unroll
;         for (int kt = 0; kt < 4; ++kt) { f32x4 p = S[c][kt] + off;
; #pragma unroll
;             for (int e = 0; e < 4; ++e) p[e] = ex2(p[e]);
;             S[c][kt] = p; }
;         pf[c][0] = pack8(S[c][0], S[c][1]); pf[c][1] = pack8(S[c][2], S[c][3]);
;         st[c].l = __builtin_amdgcn_mfma_f32_16x16x32_bf16(ONES8, pf[c][0], st[c].l, 0, 0, 0); st[c].l = __builtin_amdgcn_mfma_f32_16x16x32_bf16(ONES8, pf[c][1], st[c].l, 0, 0, 0);
;     }
; #pragma unroll
;     for (int c32 = 0; c32 < 2; ++c32)
; #pragma unroll
;         for (int dt = 0; dt < 4; ++dt) { const bf16x8 vf = lds_frag(vb, 16 * dt + col, 4 * c32 + q);
;             O[0][dt] = __builtin_amdgcn_mfma_f32_16x16x32_bf16(vf, pf[0][c32], O[0][dt], 0, 0, 0);
;             O[1][dt] = __builtin_amdgcn_mfma_f32_16x16x32_bf16(vf, pf[1][c32], O[1][dt], 0, 0, 0); }
.Lbm_r1_two:
	v_add_u32_e32 v148, s83, v192
	v_add_u32_e32 v149, v148, v195
	v_add_u32_e32 v148, v148, v193
	ds_read_b128 v[116:119], v148
	ds_read_b128 v[120:123], v149
	ds_read_b128 v[124:127], v148 offset:2048
	ds_read_b128 v[128:131], v149 offset:2048
	ds_read_b128 v[132:135], v148 offset:4096
	ds_read_b128 v[136:139], v149 offset:4096
	ds_read_b128 v[140:143], v148 offset:6144
	ds_read_b128 v[144:147], v149 offset:6144
	s_add_i32 s32, s1, 0x2000
	s_and_b32 s32, s32, 0x6000
	v_add_u32_e32 v208, s32, v192
	v_add_u32_e32 v209, v208, v195
	v_add_u32_e32 v208, v208, v193
	ds_read_b128 v[38:41], v208
	ds_read_b128 v[42:45], v209
	ds_read_b128 v[46:49], v208 offset:2048
	ds_read_b128 v[50:53], v209 offset:2048
	s_waitcnt lgkmcnt(12)
	v_sub_f32_e32 v81, v81, v199
	v_sub_f32_e32 v82, v82, v199
	v_mov_b32_e32 v70, v81
	v_mov_b32_e32 v71, v81
	v_mov_b32_e32 v72, v81
	v_mov_b32_e32 v73, v81
	v_mov_b32_e32 v74, v81
	v_mov_b32_e32 v75, v81
	v_mov_b32_e32 v76, v81
	v_mov_b32_e32 v77, v81
	v_mov_b32_e32 v200, v81
	v_mov_b32_e32 v201, v81
	v_mov_b32_e32 v202, v81
	v_mov_b32_e32 v203, v81
	v_mov_b32_e32 v204, v81
	v_mov_b32_e32 v205, v81
	v_mov_b32_e32 v206, v81
	v_mov_b32_e32 v207, v81
	v_mov_b32_e32 v54, v82
	v_mov_b32_e32 v55, v82
	v_mov_b32_e32 v56, v82
	v_mov_b32_e32 v57, v82
	v_mov_b32_e32 v58, v82
	v_mov_b32_e32 v59, v82
	v_mov_b32_e32 v60, v82
	v_mov_b32_e32 v61, v82
	v_mov_b32_e32 v62, v82
	v_mov_b32_e32 v63, v82
	v_mov_b32_e32 v64, v82
	v_mov_b32_e32 v65, v82
	v_mov_b32_e32 v66, v82
	v_mov_b32_e32 v67, v82
	v_mov_b32_e32 v68, v82
	v_mov_b32_e32 v69, v82
	s_waitcnt lgkmcnt(10)
	v_mfma_f32_16x16x32_bf16 v[70:73], v[116:119], v[104:107], v[70:73]
	v_mfma_f32_16x16x32_bf16 v[70:73], v[120:123], v[108:111], v[70:73]
	s_waitcnt lgkmcnt(8)
	v_mfma_f32_16x16x32_bf16 v[74:77], v[124:127], v[104:107], v[74:77]
	v_mfma_f32_16x16x32_bf16 v[74:77], v[128:131], v[108:111], v[74:77]
	ds_read_b128 v[116:119], v148 offset:32768
	ds_read_b128 v[120:123], v149 offset:32768
	ds_read_b128 v[124:127], v148 offset:34816
	ds_read_b128 v[128:131], v149 offset:34816
	s_waitcnt lgkmcnt(10)
	v_mfma_f32_16x16x32_bf16 v[200:203], v[132:135], v[104:107], v[200:203]
	v_mfma_f32_16x16x32_bf16 v[200:203], v[136:139], v[108:111], v[200:203]
	s_waitcnt lgkmcnt(8)
	v_mfma_f32_16x16x32_bf16 v[204:207], v[140:143], v[104:107], v[204:207]
	v_mfma_f32_16x16x32_bf16 v[204:207], v[144:147], v[108:111], v[204:207]
	ds_read_b128 v[132:135], v148 offset:36864
	ds_read_b128 v[136:139], v149 offset:36864
	ds_read_b128 v[140:143], v148 offset:38912
	ds_read_b128 v[144:147], v149 offset:38912
	s_waitcnt lgkmcnt(10)
	v_mfma_f32_16x16x32_bf16 v[54:57], v[38:41], v[104:107], v[54:57]
	v_mfma_f32_16x16x32_bf16 v[54:57], v[42:45], v[108:111], v[54:57]
	s_waitcnt lgkmcnt(8)
	v_mfma_f32_16x16x32_bf16 v[58:61], v[46:49], v[104:107], v[58:61]
	v_mfma_f32_16x16x32_bf16 v[58:61], v[50:53], v[108:111], v[58:61]
	ds_read_b128 v[38:41], v208 offset:4096
	ds_read_b128 v[42:45], v209 offset:4096
	ds_read_b128 v[46:49], v208 offset:6144
	ds_read_b128 v[50:53], v209 offset:6144
	v_exp_f32_e32 v70, v70
	v_exp_f32_e32 v71, v71
	v_exp_f32_e32 v72, v72
	v_exp_f32_e32 v73, v73
	v_exp_f32_e32 v74, v74
	v_exp_f32_e32 v75, v75
	v_exp_f32_e32 v76, v76
	v_exp_f32_e32 v77, v77
	v_exp_f32_e32 v200, v200
	v_exp_f32_e32 v201, v201
	v_exp_f32_e32 v202, v202
	v_exp_f32_e32 v203, v203
	v_exp_f32_e32 v204, v204
	v_exp_f32_e32 v205, v205
	v_exp_f32_e32 v206, v206
	v_exp_f32_e32 v207, v207
	s_nop 0
	v_cvt_pk_bf16_f32 v70, v70, v71
	v_cvt_pk_bf16_f32 v71, v72, v73
	v_cvt_pk_bf16_f32 v72, v74, v75
	v_cvt_pk_bf16_f32 v73, v76, v77
	v_cvt_pk_bf16_f32 v74, v200, v201
	v_cvt_pk_bf16_f32 v75, v202, v203
	v_cvt_pk_bf16_f32 v76, v204, v205
	v_cvt_pk_bf16_f32 v77, v206, v207
	s_nop 1
	v_mfma_f32_16x16x32_bf16 v[100:103], v[112:115], v[70:73], 0
	v_mfma_f32_16x16x32_bf16 v[100:103], v[112:115], v[74:77], v[100:103]
	s_waitcnt lgkmcnt(4)
	v_mfma_f32_16x16x32_bf16 v[84:87], v[116:119], v[70:73], 0
	v_mfma_f32_16x16x32_bf16 v[84:87], v[120:123], v[74:77], v[84:87]
	v_mfma_f32_16x16x32_bf16 v[88:91], v[124:127], v[70:73], 0
	v_mfma_f32_16x16x32_bf16 v[88:91], v[128:131], v[74:77], v[88:91]
	v_mfma_f32_16x16x32_bf16 v[92:95], v[132:135], v[70:73], 0
	v_mfma_f32_16x16x32_bf16 v[92:95], v[136:139], v[74:77], v[92:95]
	v_mfma_f32_16x16x32_bf16 v[96:99], v[140:143], v[70:73], 0
	v_mfma_f32_16x16x32_bf16 v[96:99], v[144:147], v[74:77], v[96:99]
	s_waitcnt lgkmcnt(2)
	v_mfma_f32_16x16x32_bf16 v[62:65], v[38:41], v[104:107], v[62:65]
	v_mfma_f32_16x16x32_bf16 v[62:65], v[42:45], v[108:111], v[62:65]
	s_waitcnt lgkmcnt(0)
	v_mfma_f32_16x16x32_bf16 v[66:69], v[46:49], v[104:107], v[66:69]
	v_mfma_f32_16x16x32_bf16 v[66:69], v[50:53], v[108:111], v[66:69]
	ds_read_b128 v[116:119], v208 offset:32768
	ds_read_b128 v[120:123], v209 offset:32768
	ds_read_b128 v[124:127], v208 offset:34816
	ds_read_b128 v[128:131], v209 offset:34816
	ds_read_b128 v[132:135], v208 offset:36864
	ds_read_b128 v[136:139], v209 offset:36864
	ds_read_b128 v[140:143], v208 offset:38912
	ds_read_b128 v[144:147], v209 offset:38912
	s_nop 3
	v_exp_f32_e32 v54, v54
	v_exp_f32_e32 v55, v55
	v_exp_f32_e32 v56, v56
	v_exp_f32_e32 v57, v57
	v_exp_f32_e32 v58, v58
	v_exp_f32_e32 v59, v59
	v_exp_f32_e32 v60, v60
	v_exp_f32_e32 v61, v61
	v_exp_f32_e32 v62, v62
	v_exp_f32_e32 v63, v63
	v_exp_f32_e32 v64, v64
	v_exp_f32_e32 v65, v65
	v_exp_f32_e32 v66, v66
	v_exp_f32_e32 v67, v67
	v_exp_f32_e32 v68, v68
	v_exp_f32_e32 v69, v69
	s_nop 0
	v_cvt_pk_bf16_f32 v54, v54, v55
	v_cvt_pk_bf16_f32 v55, v56, v57
	v_cvt_pk_bf16_f32 v56, v58, v59
	v_cvt_pk_bf16_f32 v57, v60, v61
	v_cvt_pk_bf16_f32 v58, v62, v63
	v_cvt_pk_bf16_f32 v59, v64, v65
	v_cvt_pk_bf16_f32 v60, v66, v67
	v_cvt_pk_bf16_f32 v61, v68, v69
	s_nop 1
	v_mfma_f32_16x16x32_bf16 v[100:103], v[112:115], v[54:57], v[100:103]
	v_mfma_f32_16x16x32_bf16 v[100:103], v[112:115], v[58:61], v[100:103]
	s_waitcnt lgkmcnt(4)
; template <bool SELMASK>
; __device__ __forceinline__ void attn_far_fast(const LAS unsigned char* kb, const LAS unsigned char* vb, const bf16x8 (&qf)[2][2], int col, int q, float bias_far, bool sel0, bool sel1, Softmax (&st)[2], f32x4 (&O)[2][4]) {
;     ...
; #pragma unroll
;     for (int c32 = 0; c32 < 2; ++c32)
; #pragma unroll
;         for (int dt = 0; dt < 4; ++dt) { const bf16x8 vf = lds_frag(vb, 16 * dt + col, 4 * c32 + q);
;             O[0][dt] = __builtin_amdgcn_mfma_f32_16x16x32_bf16(vf, pf[0][c32], O[0][dt], 0, 0, 0);
;             O[1][dt] = __builtin_amdgcn_mfma_f32_16x16x32_bf16(vf, pf[1][c32], O[1][dt], 0, 0, 0); }
	v_mfma_f32_16x16x32_bf16 v[84:87], v[116:119], v[54:57], v[84:87]
	v_mfma_f32_16x16x32_bf16 v[84:87], v[120:123], v[58:61], v[84:87]
	v_mfma_f32_16x16x32_bf16 v[88:91], v[124:127], v[54:57], v[88:91]
	v_mfma_f32_16x16x32_bf16 v[88:91], v[128:131], v[58:61], v[88:91]
	v_lshlrev_b32_e32 v254, 6, v186
	v_sub_u32_e32 v254, v83, v254
	ds_read2_b32 v[200:201], v83 offset0:0 offset1:4
	ds_read2_b32 v[202:203], v83 offset0:8 offset1:12
	ds_read2_b32 v[204:205], v83 offset0:64 offset1:68
	ds_read2_b32 v[206:207], v83 offset0:72 offset1:76
	ds_read2_b32 v[62:63], v83 offset0:128 offset1:132
	ds_read2_b32 v[64:65], v83 offset0:136 offset1:140
	ds_read2_b32 v[66:67], v83 offset0:192 offset1:196
	ds_read2_b32 v[68:69], v83 offset0:200 offset1:204
	ds_read_b32 v199, v254 offset:1024
	s_waitcnt lgkmcnt(9)
	v_mfma_f32_16x16x32_bf16 v[92:95], v[132:135], v[54:57], v[92:95]
	v_mfma_f32_16x16x32_bf16 v[92:95], v[136:139], v[58:61], v[92:95]
	v_mfma_f32_16x16x32_bf16 v[96:99], v[140:143], v[54:57], v[96:99]
	v_mfma_f32_16x16x32_bf16 v[96:99], v[144:147], v[58:61], v[96:99]
	s_nop 1
	s_waitcnt lgkmcnt(0)
	v_add_f32_e32 v200, v200, v84
	v_add_f32_e32 v201, v201, v85
	v_add_f32_e32 v202, v202, v86
	v_add_f32_e32 v203, v203, v87
	v_add_f32_e32 v204, v204, v88
	v_add_f32_e32 v205, v205, v89
	v_add_f32_e32 v206, v206, v90
	v_add_f32_e32 v207, v207, v91
	v_add_f32_e32 v199, v199, v100
	v_add_f32_e32 v62, v62, v92
	v_add_f32_e32 v63, v63, v93
	v_add_f32_e32 v64, v64, v94
	v_add_f32_e32 v65, v65, v95
	v_add_f32_e32 v66, v66, v96
	v_add_f32_e32 v67, v67, v97
	v_add_f32_e32 v68, v68, v98
	v_add_f32_e32 v69, v69, v99
	v_cmp_ne_u32_e32 vcc, 0, v79
	s_and_saveexec_b64 s[84:85], vcc
	ds_write2_b32 v83, v200, v201 offset0:0 offset1:4
	ds_write2_b32 v83, v202, v203 offset0:8 offset1:12
	ds_write2_b32 v83, v204, v205 offset0:64 offset1:68
	ds_write2_b32 v83, v206, v207 offset0:72 offset1:76
	ds_write2_b32 v83, v62, v63 offset0:128 offset1:132
	ds_write2_b32 v83, v64, v65 offset0:136 offset1:140
	ds_write2_b32 v83, v66, v67 offset0:192 offset1:196
	ds_write2_b32 v83, v68, v69 offset0:200 offset1:204
	ds_write_b32 v254, v199 offset:1024
	s_mov_b64 exec, s[84:85]
	s_nop 3
	s_mov_b32 s100, -1
	s_add_i32 s21, s91, 8
	s_andn2_b64 s[84:85], s[12:13], s[14:15]
	s_bcnt1_i32_b64 s77, s[84:85]
	v_mbcnt_lo_u32_b32 v80, s84, 0
	v_mbcnt_hi_u32_b32 v80, s85, v80
	v_mov_b32_e32 v56, s77
	s_and_b64 s[84:85], s[12:13], s[14:15]
	s_bcnt1_i32_b64 s32, s[84:85]
	v_mbcnt_lo_u32_b32 v56, s84, v56
	v_mbcnt_hi_u32_b32 v56, s85, v56
	s_add_i32 s77, s77, s32
	v_cndmask_b32_e64 v80, v80, v56, s[84:85]
	v_mov_b32_e32 v56, s77
	s_andn2_b64 s[84:85], s[14:15], s[12:13]
	v_mbcnt_lo_u32_b32 v56, s84, v56
	v_mbcnt_hi_u32_b32 v56, s85, v56
	s_nop 0
	v_cndmask_b32_e64 v80, v80, v56, s[84:85]
	v_cndmask_b32_e64 v58, 0, 1, s[12:13]
	v_cndmask_b32_e64 v59, 0, 2, s[14:15]
	v_or_b32_e32 v58, v58, v59
	v_and_b32_e32 v59, 63, v185
	v_lshl_or_b32 v58, v58, 6, v59
	s_lshl_b32 s77, s91, 6
	s_add_i32 s77, s77, 0x20900
	v_add_u32_e32 v59, s77, v80
	s_and_saveexec_b64 s[84:85], s[22:23]
	ds_write_b8 v59, v58
	s_mov_b64 exec, s[84:85]
	s_lshl_b32 s32, s21, 2
	s_bcnt1_i32_b64 s84, s[22:23]
	v_lshrrev_b32_e32 v58, 2, v250
	v_add_u32_e32 v58, s32, v58
	v_cmp_gt_u32_e32 vcc, s84, v58
	v_add_u32_e32 v59, s77, v58
	ds_read_u8 v63, v59
	v_cndmask_b32_e64 v60, -1, 0, vcc
	s_waitcnt lgkmcnt(0)
	v_or_b32_e32 v63, v63, v60
	v_lshrrev_b32_e32 v56, 31, v63
	v_xor_b32_e32 v56, 1, v56
	v_max_i32_e32 v55, 0, v63
	v_mov_b32_e32 v79, v56
	v_and_b32_e32 v54, 63, v55
	v_bfe_u32 v58, v55, 6, 1
	v_bfe_u32 v59, v55, 7, 1
	v_lshlrev_b32_e32 v60, 11, v54
	v_mov_b32_e32 v61, 0
	v_lshl_add_u64 v[60:61], v[60:61], 0, v[246:247]
	global_load_dwordx4 v[104:107], v[60:61], off
	global_load_dwordx4 v[108:111], v[60:61], off offset:64
	v_lshl_add_u32 v63, v54, 4, v249
	ds_read_b32 v199, v63
	v_mul_u32_u24_e32 v83, 0x410, v54
	v_cmp_ne_u32_e32 vcc, 0, v58
	v_add_u32_e32 v83, v83, v248
	s_nop 0
	v_cndmask_b32_e32 v81, v2, v154, vcc
	s_cmp_lg_u64 vcc, 0
	s_cselect_b32 s21, 1, 0
	v_cmp_ne_u32_e32 vcc, 0, v59
	s_nop 1
	v_cndmask_b32_e32 v82, v2, v154, vcc
	s_cmp_lg_u64 vcc, 0
	s_cselect_b32 s32, 1, 0
	s_waitcnt vmcnt(0)
	s_and_b32 s83, s1, 0x4000
	v_add_u32_e32 v148, s83, v192
	v_add_u32_e32 v149, v148, v195
	v_add_u32_e32 v148, v148, v193
	ds_read_b128 v[116:119], v148
	ds_read_b128 v[120:123], v149
	ds_read_b128 v[124:127], v148 offset:2048
	ds_read_b128 v[128:131], v149 offset:2048
	ds_read_b128 v[132:135], v148 offset:4096
	ds_read_b128 v[136:139], v149 offset:4096
	ds_read_b128 v[140:143], v148 offset:6144
	ds_read_b128 v[144:147], v149 offset:6144
	s_add_i32 s32, s1, 0x2000
	s_and_b32 s32, s32, 0x6000
	v_add_u32_e32 v208, s32, v192
	v_add_u32_e32 v209, v208, v195
	v_add_u32_e32 v208, v208, v193
	ds_read_b128 v[38:41], v208
	ds_read_b128 v[42:45], v209
	ds_read_b128 v[46:49], v208 offset:2048
	ds_read_b128 v[50:53], v209 offset:2048
	s_waitcnt lgkmcnt(12)
	v_sub_f32_e32 v81, v81, v199
	v_sub_f32_e32 v82, v82, v199
	v_mov_b32_e32 v70, v81
	v_mov_b32_e32 v71, v81
	v_mov_b32_e32 v72, v81
	v_mov_b32_e32 v73, v81
	v_mov_b32_e32 v74, v81
	v_mov_b32_e32 v75, v81
	v_mov_b32_e32 v76, v81
	v_mov_b32_e32 v77, v81
	v_mov_b32_e32 v200, v81
	v_mov_b32_e32 v201, v81
	v_mov_b32_e32 v202, v81
	v_mov_b32_e32 v203, v81
	v_mov_b32_e32 v204, v81
	v_mov_b32_e32 v205, v81
	v_mov_b32_e32 v206, v81
	v_mov_b32_e32 v207, v81
	v_mov_b32_e32 v54, v82
	v_mov_b32_e32 v55, v82
	v_mov_b32_e32 v56, v82
	v_mov_b32_e32 v57, v82
	v_mov_b32_e32 v58, v82
	v_mov_b32_e32 v59, v82
	v_mov_b32_e32 v60, v82
	v_mov_b32_e32 v61, v82
	v_mov_b32_e32 v62, v82
	v_mov_b32_e32 v63, v82
	v_mov_b32_e32 v64, v82
	v_mov_b32_e32 v65, v82
	v_mov_b32_e32 v66, v82
	v_mov_b32_e32 v67, v82
	v_mov_b32_e32 v68, v82
	v_mov_b32_e32 v69, v82
	s_waitcnt lgkmcnt(10)
; __device__ __forceinline__ float ex2(float x) { return __builtin_amdgcn_exp2f(x); }
; template <bool SELMASK>
; __device__ __forceinline__ void attn_far_fast(const LAS unsigned char* kb, const LAS unsigned char* vb, const bf16x8 (&qf)[2][2], int col, int q, float bias_far, bool sel0, bool sel1, Softmax (&st)[2], f32x4 (&O)[2][4]) {
;     ...
; #pragma unroll
;     for (int kt = 0; kt < 4; ++kt) { const bf16x8 k0 = lds_frag(kb, 16 * kt + col, q), k1 = lds_frag(kb, 16 * kt + col, 4 + q);
; #pragma unroll
;         for (int c = 0; c < 2; ++c) { S[c][kt] = __builtin_amdgcn_mfma_f32_16x16x32_bf16(k0, qf[c][0], z4, 0, 0, 0); S[c][kt] = __builtin_amdgcn_mfma_f32_16x16x32_bf16(k1, qf[c][1], S[c][kt], 0, 0, 0); } }
;     bf16x8 pf[2][2];
; #pragma unroll
;     for (int c = 0; c < 2; ++c) {
;         const bool sel = c == 0 ? sel0 : sel1;
;         const float off = ((SELMASK && !sel) ? NEG : bias_far) - st[c].m;
; #pragma unroll
;         for (int kt = 0; kt < 4; ++kt) { f32x4 p = S[c][kt] + off;
; #pragma unroll
;             for (int e = 0; e < 4; ++e) p[e] = ex2(p[e]);
;             S[c][kt] = p; }
;         pf[c][0] = pack8(S[c][0], S[c][1]); pf[c][1] = pack8(S[c][2], S[c][3]);
;         st[c].l = __builtin_amdgcn_mfma_f32_16x16x32_bf16(ONES8, pf[c][0], st[c].l, 0, 0, 0); st[c].l = __builtin_amdgcn_mfma_f32_16x16x32_bf16(ONES8, pf[c][1], st[c].l, 0, 0, 0);
;     }
; #pragma unroll
;     for (int c32 = 0; c32 < 2; ++c32)
; #pragma unroll
;         for (int dt = 0; dt < 4; ++dt) { const bf16x8 vf = lds_frag(vb, 16 * dt + col, 4 * c32 + q);
;             O[0][dt] = __builtin_amdgcn_mfma_f32_16x16x32_bf16(vf, pf[0][c32], O[0][dt], 0, 0, 0);
;             O[1][dt] = __builtin_amdgcn_mfma_f32_16x16x32_bf16(vf, pf[1][c32], O[1][dt], 0, 0, 0); }
	v_mfma_f32_16x16x32_bf16 v[70:73], v[116:119], v[104:107], v[70:73]
	v_mfma_f32_16x16x32_bf16 v[70:73], v[120:123], v[108:111], v[70:73]
	s_waitcnt lgkmcnt(8)
	v_mfma_f32_16x16x32_bf16 v[74:77], v[124:127], v[104:107], v[74:77]
	v_mfma_f32_16x16x32_bf16 v[74:77], v[128:131], v[108:111], v[74:77]
	ds_read_b128 v[116:119], v148 offset:32768
	ds_read_b128 v[120:123], v149 offset:32768
	ds_read_b128 v[124:127], v148 offset:34816
	ds_read_b128 v[128:131], v149 offset:34816
	s_waitcnt lgkmcnt(10)
	v_mfma_f32_16x16x32_bf16 v[200:203], v[132:135], v[104:107], v[200:203]
	v_mfma_f32_16x16x32_bf16 v[200:203], v[136:139], v[108:111], v[200:203]
	s_waitcnt lgkmcnt(8)
	v_mfma_f32_16x16x32_bf16 v[204:207], v[140:143], v[104:107], v[204:207]
	v_mfma_f32_16x16x32_bf16 v[204:207], v[144:147], v[108:111], v[204:207]
	ds_read_b128 v[132:135], v148 offset:36864
	ds_read_b128 v[136:139], v149 offset:36864
	ds_read_b128 v[140:143], v148 offset:38912
	ds_read_b128 v[144:147], v149 offset:38912
	s_waitcnt lgkmcnt(10)
	v_mfma_f32_16x16x32_bf16 v[54:57], v[38:41], v[104:107], v[54:57]
	v_mfma_f32_16x16x32_bf16 v[54:57], v[42:45], v[108:111], v[54:57]
	s_waitcnt lgkmcnt(8)
	v_mfma_f32_16x16x32_bf16 v[58:61], v[46:49], v[104:107], v[58:61]
	v_mfma_f32_16x16x32_bf16 v[58:61], v[50:53], v[108:111], v[58:61]
	ds_read_b128 v[38:41], v208 offset:4096
	ds_read_b128 v[42:45], v209 offset:4096
	ds_read_b128 v[46:49], v208 offset:6144
	ds_read_b128 v[50:53], v209 offset:6144
	v_exp_f32_e32 v70, v70
	v_exp_f32_e32 v71, v71
	v_exp_f32_e32 v72, v72
	v_exp_f32_e32 v73, v73
	v_exp_f32_e32 v74, v74
	v_exp_f32_e32 v75, v75
	v_exp_f32_e32 v76, v76
	v_exp_f32_e32 v77, v77
	v_exp_f32_e32 v200, v200
	v_exp_f32_e32 v201, v201
	v_exp_f32_e32 v202, v202
	v_exp_f32_e32 v203, v203
	v_exp_f32_e32 v204, v204
	v_exp_f32_e32 v205, v205
	v_exp_f32_e32 v206, v206
	v_exp_f32_e32 v207, v207
	s_nop 0
	v_cvt_pk_bf16_f32 v70, v70, v71
	v_cvt_pk_bf16_f32 v71, v72, v73
	v_cvt_pk_bf16_f32 v72, v74, v75
	v_cvt_pk_bf16_f32 v73, v76, v77
	v_cvt_pk_bf16_f32 v74, v200, v201
	v_cvt_pk_bf16_f32 v75, v202, v203
	v_cvt_pk_bf16_f32 v76, v204, v205
	v_cvt_pk_bf16_f32 v77, v206, v207
	s_nop 1
	v_mfma_f32_16x16x32_bf16 v[100:103], v[112:115], v[70:73], 0
	v_mfma_f32_16x16x32_bf16 v[100:103], v[112:115], v[74:77], v[100:103]
	s_waitcnt lgkmcnt(4)
	v_mfma_f32_16x16x32_bf16 v[84:87], v[116:119], v[70:73], 0
	v_mfma_f32_16x16x32_bf16 v[84:87], v[120:123], v[74:77], v[84:87]
	v_mfma_f32_16x16x32_bf16 v[88:91], v[124:127], v[70:73], 0
	v_mfma_f32_16x16x32_bf16 v[88:91], v[128:131], v[74:77], v[88:91]
	v_mfma_f32_16x16x32_bf16 v[92:95], v[132:135], v[70:73], 0
	v_mfma_f32_16x16x32_bf16 v[92:95], v[136:139], v[74:77], v[92:95]
	v_mfma_f32_16x16x32_bf16 v[96:99], v[140:143], v[70:73], 0
	v_mfma_f32_16x16x32_bf16 v[96:99], v[144:147], v[74:77], v[96:99]
	s_waitcnt lgkmcnt(2)
	v_mfma_f32_16x16x32_bf16 v[62:65], v[38:41], v[104:107], v[62:65]
	v_mfma_f32_16x16x32_bf16 v[62:65], v[42:45], v[108:111], v[62:65]
	s_waitcnt lgkmcnt(0)
	v_mfma_f32_16x16x32_bf16 v[66:69], v[46:49], v[104:107], v[66:69]
	v_mfma_f32_16x16x32_bf16 v[66:69], v[50:53], v[108:111], v[66:69]
	ds_read_b128 v[116:119], v208 offset:32768
	ds_read_b128 v[120:123], v209 offset:32768
	ds_read_b128 v[124:127], v208 offset:34816
	ds_read_b128 v[128:131], v209 offset:34816
	ds_read_b128 v[132:135], v208 offset:36864
	ds_read_b128 v[136:139], v209 offset:36864
	ds_read_b128 v[140:143], v208 offset:38912
	ds_read_b128 v[144:147], v209 offset:38912
	s_nop 3
	v_exp_f32_e32 v54, v54
	v_exp_f32_e32 v55, v55
	v_exp_f32_e32 v56, v56
	v_exp_f32_e32 v57, v57
	v_exp_f32_e32 v58, v58
	v_exp_f32_e32 v59, v59
	v_exp_f32_e32 v60, v60
	v_exp_f32_e32 v61, v61
	v_exp_f32_e32 v62, v62
	v_exp_f32_e32 v63, v63
	v_exp_f32_e32 v64, v64
	v_exp_f32_e32 v65, v65
	v_exp_f32_e32 v66, v66
	v_exp_f32_e32 v67, v67
	v_exp_f32_e32 v68, v68
	v_exp_f32_e32 v69, v69
	s_nop 0
	v_cvt_pk_bf16_f32 v54, v54, v55
	v_cvt_pk_bf16_f32 v55, v56, v57
	v_cvt_pk_bf16_f32 v56, v58, v59
	v_cvt_pk_bf16_f32 v57, v60, v61
	v_cvt_pk_bf16_f32 v58, v62, v63
	v_cvt_pk_bf16_f32 v59, v64, v65
	v_cvt_pk_bf16_f32 v60, v66, v67
	v_cvt_pk_bf16_f32 v61, v68, v69
	s_nop 1
	v_mfma_f32_16x16x32_bf16 v[100:103], v[112:115], v[54:57], v[100:103]
	v_mfma_f32_16x16x32_bf16 v[100:103], v[112:115], v[58:61], v[100:103]
	s_waitcnt lgkmcnt(4)
	v_mfma_f32_16x16x32_bf16 v[84:87], v[116:119], v[54:57], v[84:87]
	v_mfma_f32_16x16x32_bf16 v[84:87], v[120:123], v[58:61], v[84:87]
	v_mfma_f32_16x16x32_bf16 v[88:91], v[124:127], v[54:57], v[88:91]
	v_mfma_f32_16x16x32_bf16 v[88:91], v[128:131], v[58:61], v[88:91]
	v_lshlrev_b32_e32 v254, 6, v186
	v_sub_u32_e32 v254, v83, v254
	ds_read2_b32 v[200:201], v83 offset0:0 offset1:4
	ds_read2_b32 v[202:203], v83 offset0:8 offset1:12
	ds_read2_b32 v[204:205], v83 offset0:64 offset1:68
	ds_read2_b32 v[206:207], v83 offset0:72 offset1:76
	ds_read2_b32 v[62:63], v83 offset0:128 offset1:132
	ds_read2_b32 v[64:65], v83 offset0:136 offset1:140
	ds_read2_b32 v[66:67], v83 offset0:192 offset1:196
	ds_read2_b32 v[68:69], v83 offset0:200 offset1:204
	ds_read_b32 v199, v254 offset:1024
	s_waitcnt lgkmcnt(9)
	v_mfma_f32_16x16x32_bf16 v[92:95], v[132:135], v[54:57], v[92:95]
	v_mfma_f32_16x16x32_bf16 v[92:95], v[136:139], v[58:61], v[92:95]
	v_mfma_f32_16x16x32_bf16 v[96:99], v[140:143], v[54:57], v[96:99]
	v_mfma_f32_16x16x32_bf16 v[96:99], v[144:147], v[58:61], v[96:99]
	s_nop 1
	s_waitcnt lgkmcnt(0)
	v_add_f32_e32 v200, v200, v84
	v_add_f32_e32 v201, v201, v85
	v_add_f32_e32 v202, v202, v86
	v_add_f32_e32 v203, v203, v87
	v_add_f32_e32 v204, v204, v88
	v_add_f32_e32 v205, v205, v89
	v_add_f32_e32 v206, v206, v90
	v_add_f32_e32 v207, v207, v91
	v_add_f32_e32 v199, v199, v100
	v_add_f32_e32 v62, v62, v92
	v_add_f32_e32 v63, v63, v93
	v_add_f32_e32 v64, v64, v94
	v_add_f32_e32 v65, v65, v95
	v_add_f32_e32 v66, v66, v96
	v_add_f32_e32 v67, v67, v97
	v_add_f32_e32 v68, v68, v98
	v_add_f32_e32 v69, v69, v99
	v_cmp_ne_u32_e32 vcc, 0, v79
	s_and_saveexec_b64 s[84:85], vcc
	ds_write2_b32 v83, v200, v201 offset0:0 offset1:4
	ds_write2_b32 v83, v202, v203 offset0:8 offset1:12
	ds_write2_b32 v83, v204, v205 offset0:64 offset1:68
	ds_write2_b32 v83, v206, v207 offset0:72 offset1:76
	ds_write2_b32 v83, v62, v63 offset0:128 offset1:132
	ds_write2_b32 v83, v64, v65 offset0:136 offset1:140
	ds_write2_b32 v83, v66, v67 offset0:192 offset1:196
	ds_write2_b32 v83, v68, v69 offset0:200 offset1:204
	ds_write_b32 v254, v199 offset:1024
	s_mov_b64 exec, s[84:85]
	s_nop 3

.Lbm_g2_end_nb:
.Lbm_join:
	s_add_i32 s10, s1, 0x4000
	s_and_b32 s10, s10, 0x4000
	v_add_u32_e32 v78, s10, v188
	s_add_i32 s10, s1, 0x6000
	s_and_b32 s10, s10, 0x6000
	v_add_u32_e32 v79, s10, v188
	s_cmp_lt_i32 s100, 0
	s_cselect_b32 s10, 0, 2
	s_cmp_eq_u32 s99, 2
	s_cselect_b32 s11, 4, 0
	s_add_i32 s10, s10, s11
	s_cmp_eq_u32 s99, 3
	s_cselect_b32 s11, 4, 0
	s_add_i32 s10, s10, s11
	s_cmp_eq_u32 s10, 0
	s_cbranch_scc1 .Lbm_jw0
	s_cmp_eq_u32 s10, 2
	s_cbranch_scc1 .Lbm_jw2
	s_cmp_eq_u32 s10, 4
	s_cbranch_scc1 .Lbm_jw4
	s_waitcnt vmcnt(6)
	s_branch .Lbm_jwd
.Lbm_jw4:
	s_waitcnt vmcnt(4)
	s_branch .Lbm_jwd
.Lbm_jw2:
	s_waitcnt vmcnt(2)
	s_branch .Lbm_jwd

; __device__ __forceinline__ void nsa_unit(unsigned char* ws, LAS unsigned char* lds, const LAS float* lut, int b, int g, int tau, int tid_in) {
;     ...
;     for (int c = 0; c < 2; ++c) { tq[c] = t0 + 8 * wave + 4 * c + tl; const size_t qrow = (size_t)b * SEQ + tq[c];
;         const bf16_t* Qp = (const bf16_t*)(ws + WS_Q) + qrow * 1024 + h * 64 + 8 * q; qf[c][0] = *(const bf16x8*)Qp; qf[c][1] = *(const bf16x8*)(Qp + 32); }
.Lbm_jwd:
	s_cmp_ge_u32 s99, 3
	s_cbranch_scc1 .Lbm_jB
	ds_write_b128 v78, v[26:29]
	ds_write_b128 v78, v[22:25] offset:32768
	ds_write_b128 v79, v[30:33]
	ds_write_b128 v79, v[34:37] offset:32768
	s_add_i32 s10, s26, -4
	s_cmp_eq_u32 s99, 2
	s_cbranch_scc1 .Lbm_jA2
	s_mov_b32 s99, 0
	s_mov_b32 s101, 4
	s_add_i32 s11, s75, 2
	s_cmp_le_i32 s11, s26
	s_cbranch_scc1 .Lbm_jA1
	s_lshl_b32 s11, s91, 3
	v_add_u32_e32 v82, s11, v184
	v_lshlrev_b32_e32 v82, 11, v82
	v_mov_b32_e32 v83, 0
	v_lshl_add_u64 v[82:83], v[82:83], 0, v[246:247]
	v_add_co_u32_e32 v254, vcc, 0x2000, v82
	s_nop 1
	v_addc_co_u32_e32 v255, vcc, 0, v83, vcc
	global_load_dwordx4 v[6:9], v[82:83], off
	global_load_dwordx4 v[10:13], v[82:83], off offset:64
	global_load_dwordx4 v[14:17], v[254:255], off
	global_load_dwordx4 v[18:21], v[254:255], off offset:64
.Lbm_jA1:
	s_cmp_ge_i32 s75, s26
	s_cbranch_scc1 .LBB0_1228
	s_add_u32 s12, s64, 0x10000
	s_addc_u32 s13, s65, 0
	s_add_u32 s14, s62, 0x100
	s_addc_u32 s15, s63, 0
	v_lshl_add_u64 v[78:79], s[14:15], 0, v[162:163]
	v_lshl_add_u64 v[80:81], s[12:13], 0, v[156:157]
	v_lshl_add_u64 v[82:83], s[12:13], 0, v[166:167]
	v_lshl_add_u64 v[254:255], s[14:15], 0, v[168:169]
	v_lshl_add_u64 v[78:79], v[78:79], 0, v[160:161]
	v_lshl_add_u64 v[80:81], v[80:81], 0, v[160:161]
	v_add_co_u32_e32 v82, vcc, 0x8000, v82
	s_nop 1
	v_addc_co_u32_e32 v83, vcc, 0, v83, vcc
	global_load_dwordx4 v[22:25], v[78:79], off
	global_load_dwordx4 v[26:29], v[80:81], off
	global_load_dwordx4 v[30:33], v[82:83], off
	global_load_dwordx4 v[34:37], v[254:255], off offset:128
	s_mov_b32 s99, 1
	s_cmp_gt_i32 s75, s10
	s_cbranch_scc1 .LBB0_1228
	s_add_u32 s12, s64, 0x20000
	s_addc_u32 s13, s65, 0
	s_add_u32 s14, s62, 0x200
	s_addc_u32 s15, s63, 0
	v_lshl_add_u64 v[78:79], s[14:15], 0, v[162:163]
	v_lshl_add_u64 v[80:81], s[12:13], 0, v[156:157]
	v_lshl_add_u64 v[82:83], s[12:13], 0, v[166:167]
	v_lshl_add_u64 v[254:255], s[14:15], 0, v[168:169]
	v_lshl_add_u64 v[78:79], v[78:79], 0, v[160:161]
	v_lshl_add_u64 v[80:81], v[80:81], 0, v[160:161]
	v_add_co_u32_e32 v82, vcc, 0x8000, v82
	s_nop 1
	v_addc_co_u32_e32 v83, vcc, 0, v83, vcc
	global_load_dwordx4 v[6:9], v[78:79], off
	global_load_dwordx4 v[10:13], v[80:81], off
	global_load_dwordx4 v[14:17], v[82:83], off
	global_load_dwordx4 v[18:21], v[254:255], off offset:128
	s_mov_b32 s99, 2
	s_mov_b32 s101, 8
	s_branch .LBB0_1228
.Lbm_jA2:
	s_mov_b32 s99, 4
	s_mov_b32 s101, 0
	s_cmp_gt_i32 s75, s10
	s_cbranch_scc1 .LBB0_1228
	s_add_u32 s12, s64, 0x20000
	s_addc_u32 s13, s65, 0
	s_add_u32 s14, s62, 0x200
	s_addc_u32 s15, s63, 0
	v_lshl_add_u64 v[78:79], s[14:15], 0, v[162:163]
	v_lshl_add_u64 v[80:81], s[12:13], 0, v[156:157]
	v_lshl_add_u64 v[82:83], s[12:13], 0, v[166:167]
	v_lshl_add_u64 v[254:255], s[14:15], 0, v[168:169]
	v_lshl_add_u64 v[78:79], v[78:79], 0, v[160:161]
	v_lshl_add_u64 v[80:81], v[80:81], 0, v[160:161]
	v_add_co_u32_e32 v82, vcc, 0x8000, v82
	s_nop 1
	v_addc_co_u32_e32 v83, vcc, 0, v83, vcc
	global_load_dwordx4 v[22:25], v[78:79], off
	global_load_dwordx4 v[26:29], v[80:81], off
	global_load_dwordx4 v[30:33], v[82:83], off
	global_load_dwordx4 v[34:37], v[254:255], off offset:128
	s_mov_b32 s99, 3
	s_mov_b32 s101, 4
	s_branch .LBB0_1228
.Lbm_jB:
	ds_write_b128 v78, v[10:13]
	ds_write_b128 v78, v[6:9] offset:32768
	ds_write_b128 v79, v[14:17]
	ds_write_b128 v79, v[18:21] offset:32768
	s_add_i32 s10, s26, -4
	s_cmp_eq_u32 s99, 3
	s_cbranch_scc1 .Lbm_jB3
	s_mov_b32 s99, 0
	s_mov_b32 s101, 4
	s_add_i32 s11, s75, 2
	s_cmp_le_i32 s11, s26
	s_cbranch_scc1 .Lbm_jB1
	s_lshl_b32 s11, s91, 3
	v_add_u32_e32 v82, s11, v184
	v_lshlrev_b32_e32 v82, 11, v82
	v_mov_b32_e32 v83, 0
	v_lshl_add_u64 v[82:83], v[82:83], 0, v[246:247]
	v_add_co_u32_e32 v254, vcc, 0x2000, v82
	s_nop 1
	v_addc_co_u32_e32 v255, vcc, 0, v83, vcc
	global_load_dwordx4 v[6:9], v[82:83], off
	global_load_dwordx4 v[10:13], v[82:83], off offset:64
	global_load_dwordx4 v[14:17], v[254:255], off
	global_load_dwordx4 v[18:21], v[254:255], off offset:64
.Lbm_jB1:
	s_cmp_ge_i32 s75, s26
	s_cbranch_scc1 .LBB0_1228
	s_add_u32 s12, s64, 0x10000
	s_addc_u32 s13, s65, 0
	s_add_u32 s14, s62, 0x100
	s_addc_u32 s15, s63, 0
	v_lshl_add_u64 v[78:79], s[14:15], 0, v[162:163]
	v_lshl_add_u64 v[80:81], s[12:13], 0, v[156:157]
	v_lshl_add_u64 v[82:83], s[12:13], 0, v[166:167]
	v_lshl_add_u64 v[254:255], s[14:15], 0, v[168:169]
	v_lshl_add_u64 v[78:79], v[78:79], 0, v[160:161]
	v_lshl_add_u64 v[80:81], v[80:81], 0, v[160:161]
	v_add_co_u32_e32 v82, vcc, 0x8000, v82
	s_nop 1
	v_addc_co_u32_e32 v83, vcc, 0, v83, vcc
	global_load_dwordx4 v[22:25], v[78:79], off
	global_load_dwordx4 v[26:29], v[80:81], off
	global_load_dwordx4 v[30:33], v[82:83], off
	global_load_dwordx4 v[34:37], v[254:255], off offset:128
	s_mov_b32 s99, 1
	s_branch .LBB0_1228
.Lbm_jB3:
	s_mov_b32 s99, 1
	s_mov_b32 s101, 0
	s_cmp_gt_i32 s75, s10
	s_cbranch_scc1 .LBB0_1228
	s_add_u32 s12, s64, 0x20000
	s_addc_u32 s13, s65, 0
	s_add_u32 s14, s62, 0x200
	s_addc_u32 s15, s63, 0
	v_lshl_add_u64 v[78:79], s[14:15], 0, v[162:163]
	v_lshl_add_u64 v[80:81], s[12:13], 0, v[156:157]
	v_lshl_add_u64 v[82:83], s[12:13], 0, v[166:167]
	v_lshl_add_u64 v[254:255], s[14:15], 0, v[168:169]
	v_lshl_add_u64 v[78:79], v[78:79], 0, v[160:161]
	v_lshl_add_u64 v[80:81], v[80:81], 0, v[160:161]
	v_add_co_u32_e32 v82, vcc, 0x8000, v82
	s_nop 1
	v_addc_co_u32_e32 v83, vcc, 0, v83, vcc
	global_load_dwordx4 v[6:9], v[78:79], off
	global_load_dwordx4 v[10:13], v[80:81], off
	global_load_dwordx4 v[14:17], v[82:83], off
	global_load_dwordx4 v[18:21], v[254:255], off offset:128
	s_mov_b32 s99, 2
	s_mov_b32 s101, 4
	s_branch .LBB0_1228
